# baseline (speedup 1.0000x reference)
.LBB0_14:
	s_andn2_b64 vcc, exec, s[4:5]
	s_cbranch_vccnz .LBB0_28
	s_waitcnt lgkmcnt(0)
	s_load_dwordx2 s[6:7], s[0:1], 0x0
	s_movk_i32 s3, 0x187
	v_cmp_gt_u32_e32 vcc, s3, v0
	v_lshlrev_b32_e32 v1, 2, v0
	s_and_saveexec_b64 s[4:5], vcc
	v_mov_b32_e32 v2, 0
	ds_write_b32 v1, v2
	s_or_b64 exec, exec, s[4:5]
	s_mul_i32 s3, s2, 0x186a
	v_add_u32_e32 v2, s3, v0
	v_mov_b32_e32 v3, 0
	v_add_u32_e32 v4, 0x400, v2
	v_mov_b32_e32 v5, v3
	s_waitcnt lgkmcnt(0)
	v_lshl_add_u64 v[12:13], v[4:5], 2, s[6:7]
	v_add_u32_e32 v4, 0x800, v2
	v_lshl_add_u64 v[14:15], v[4:5], 2, s[6:7]
	v_add_u32_e32 v4, 0xc00, v2
	v_lshl_add_u64 v[10:11], v[2:3], 2, s[6:7]
	v_lshl_add_u64 v[16:17], v[4:5], 2, s[6:7]
	v_add_u32_e32 v4, 0x1000, v2
	v_add_u32_e32 v2, 0x1400, v2
	v_lshl_add_u64 v[18:19], v[4:5], 2, s[6:7]
	v_lshl_add_u64 v[20:21], v[2:3], 2, s[6:7]
	global_load_dword v9, v[10:11], off
	global_load_dword v8, v[12:13], off
	global_load_dword v7, v[14:15], off
	global_load_dword v6, v[16:17], off
	global_load_dword v5, v[18:19], off
	global_load_dword v4, v[20:21], off
	s_barrier
	s_movk_i32 s4, 0x186a
	v_or_b32_e32 v10, 0x1800, v0
	v_cmp_gt_u32_e64 s[4:5], s4, v10
	v_mov_b32_e32 v2, -1
	s_and_saveexec_b64 s[8:9], s[4:5]
	s_cbranch_execnz .LBB0_29
	s_or_b64 exec, exec, s[8:9]
	s_waitcnt vmcnt(5)
	v_cmp_lt_i32_e64 s[4:5], -1, v9
	s_and_saveexec_b64 s[6:7], s[4:5]
	s_cbranch_execnz .LBB0_30

.Lc7_nox:
	s_or_b64 exec, exec, s[38:39]
	s_waitcnt lgkmcnt(0)
	s_load_dwordx4 s[12:15], s[0:1], 0x0
	s_mov_b32 s3, 0
	s_lshl_b64 s[4:5], s[2:3], 2
	s_movk_i32 s3, 0x100
	v_cmp_gt_u32_e32 vcc, s3, v0
	s_waitcnt lgkmcnt(0)
	s_add_u32 s4, s12, s4
	s_addc_u32 s5, s13, s5
	s_load_dwordx2 s[16:17], s[4:5], 0x0
	s_and_saveexec_b64 s[4:5], vcc
	v_lshlrev_b32_e32 v1, 2, v0
	v_mov_b32_e32 v2, 0
	ds_write_b32 v1, v2 offset:4864
	s_or_b64 exec, exec, s[4:5]
	s_waitcnt lgkmcnt(0)
	v_add_u32_e32 v2, s16, v0
	v_cmp_gt_i32_e64 s[4:5], s17, v2
	v_mov_b32_e32 v8, -1
	v_mov_b32_e32 v9, -1
	s_waitcnt vmcnt(0)
	s_and_saveexec_b64 s[6:7], s[4:5]
	s_cbranch_execz .LBB2_5
	v_ashrrev_i32_e32 v3, 31, v2
	v_lshl_add_u64 v[4:5], v[2:3], 2, s[14:15]
	global_load_dword v9, v[4:5], off

.Lc7_cnt:
	s_barrier
	v_cmp_lt_i32_e64 s[10:11], -1, v9
	s_and_saveexec_b64 s[4:5], s[10:11]
	s_cbranch_execnz .LBB2_49
